# RWKV bonus scalar now produced in P4a (per token, head) and consumed in P5: P5 no longer re-reads r, k, iclr from HBM; plus P4b in-register scan state
# speedup vs baseline: 1.0042x; 1.0042x over previous
; __device__ __forceinline__ void p4a_chunk(Frame& F0, const In& I) {
;     ...
;     for (int unit = F.vcu; unit < BATCH * RH * (SEQ / 64); unit += F.G, ++uit) {
;         const int bh = unit >> 7, ck = unit & 127, b = bh >> 4, h = bh & 15;
;         const size_t tok0 = (size_t)b * SEQ + (size_t)ck * 64 + 8 * w;
;         const int hc = h * 64 + lane;
;         float lwv[8], ic[8], rr[8], kk[8], vv[8];
; #pragma unroll
;         for (int i = 0; i < 8; ++i) { const size_t tok = tok0 + i; lwv[i] = LW[tok * RW + hc]; ic[i] = bf2f(ICL[tok * RW + hc]);
;             rr[i] = bf2f(RKV[tok * (3 * RW) + hc]); kk[i] = bf2f(RKV[tok * (3 * RW) + RW + hc]); vv[i] = bf2f(RKV[tok * (3 * RW) + 2 * RW + hc]); }
;         const float kkp = I.k_k[hc], kap = I.k_a[hc];
.LBB0_1083:
	s_ashr_i32 s14, s13, 11
	s_ashr_i32 s15, s14, 31
	s_lshl_b64 s[14:15], s[14:15], 13
	s_and_b32 s16, s33, 0x1fc0
	s_add_u32 s16, s16, s22
	s_addc_u32 s17, 0, s23
	s_add_u32 s14, s16, s14
	s_addc_u32 s15, s17, s15
	s_lshr_b32 s16, s13, 1
	s_and_b32 s16, s16, 0x3c0
	s_waitcnt vmcnt(8)
	v_readlane_b32 s56, v254, 27
	v_readlane_b32 s57, v254, 28
	v_or_b32_e32 v88, s16, v1
	s_lshl_b64 s[16:17], s[14:15], 10
	v_or_b32_e32 v82, s16, v88
	s_mulk_i32 s15, 0x1800
	s_mul_hi_u32 s16, s14, 0x1800
	v_mov_b32_e32 v83, s17
	s_add_i32 s16, s16, s15
	s_mulk_i32 s14, 0x1800
	v_readlane_b32 s20, v254, 54
	v_lshl_add_u64 v[80:81], v[82:83], 2, s[0:1]
	v_readlane_b32 s21, v254, 55
	s_add_u32 s14, s20, s14
	global_load_dword v89, v[80:81], off
	v_lshl_add_u64 v[80:81], v[82:83], 1, s[88:89]
	s_addc_u32 s15, s21, s16
	v_lshlrev_b32_e32 v68, 1, v88
	global_load_ushort v84, v[80:81], off
	v_lshl_add_u64 v[80:81], s[14:15], 0, v[68:69]
	global_load_ushort v90, v68, s[14:15]
	global_load_ushort v85, v68, s[14:15] offset:2048
	s_movk_i32 s14, 0x1000
	v_add_co_u32_e32 v86, vcc, s14, v80
	s_mov_b64 s[14:15], 0x400
	v_lshl_add_u64 v[92:93], v[82:83], 0, s[14:15]
	v_addc_co_u32_e32 v87, vcc, 0, v81, vcc
	v_lshl_add_u64 v[94:95], v[92:93], 2, s[0:1]
	v_lshl_add_u64 v[92:93], v[92:93], 1, s[88:89]
	s_movk_i32 s14, 0x2000
	global_load_ushort v168, v[86:87], off
	v_readlane_b32 s48, v254, 21
	global_load_dword v94, v[94:95], off
	v_lshlrev_b32_e32 v68, 2, v88
	global_load_ushort v95, v[92:93], off
	v_lshl_add_u64 v[92:93], v[80:81], 0, s[78:79]
	global_load_ushort v96, v[86:87], off offset:2048
	global_load_ushort v91, v[92:93], off offset:2048
	v_add_co_u32_e32 v86, vcc, s14, v80
	s_mov_b64 s[14:15], 0x800
	s_nop 0
	v_addc_co_u32_e32 v87, vcc, 0, v81, vcc
	global_load_ushort v169, v[86:87], off offset:2048
	v_lshl_add_u64 v[86:87], v[82:83], 0, s[14:15]
	v_lshl_add_u64 v[92:93], v[86:87], 2, s[0:1]
	v_lshl_add_u64 v[86:87], v[86:87], 1, s[88:89]
	s_mov_b64 s[14:15], 0x3000
	global_load_dword v104, v[92:93], off
	global_load_ushort v97, v[86:87], off
	v_lshl_add_u64 v[86:87], v[80:81], 0, s[14:15]
	s_movk_i32 s14, 0x4000
	v_add_co_u32_e32 v92, vcc, s14, v80
	s_mov_b64 s[14:15], 0xc00
	s_nop 0
	v_addc_co_u32_e32 v93, vcc, 0, v81, vcc
	global_load_ushort v99, v[92:93], off offset:-4096
	global_load_ushort v98, v[86:87], off offset:2048
	global_load_ushort v170, v[92:93], off
	v_lshl_add_u64 v[86:87], v[82:83], 0, s[14:15]
	v_lshl_add_u64 v[100:101], v[86:87], 2, s[0:1]
	v_lshl_add_u64 v[86:87], v[86:87], 1, s[88:89]
	s_mov_b64 s[14:15], 0x4800
	global_load_dword v105, v[100:101], off
	global_load_ushort v102, v[86:87], off
	v_lshl_add_u64 v[86:87], v[80:81], 0, s[14:15]
	s_movk_i32 s14, 0x5000
	global_load_ushort v106, v[92:93], off offset:2048
	global_load_ushort v103, v[86:87], off offset:2048
	v_add_co_u32_e32 v86, vcc, s14, v80
	s_mov_b64 s[14:15], 0x1000
	s_nop 0
	v_addc_co_u32_e32 v87, vcc, 0, v81, vcc
	global_load_ushort v171, v[86:87], off offset:2048
	v_lshl_add_u64 v[86:87], v[82:83], 0, s[14:15]
	v_lshl_add_u64 v[92:93], v[86:87], 2, s[0:1]
	v_lshl_add_u64 v[86:87], v[86:87], 1, s[88:89]
	s_mov_b64 s[14:15], 0x6000
	global_load_dword v108, v[92:93], off
	global_load_ushort v110, v[86:87], off
	v_lshl_add_u64 v[86:87], v[80:81], 0, s[14:15]
	s_movk_i32 s14, 0x7000
	v_add_co_u32_e32 v92, vcc, s14, v80
	s_mov_b64 s[14:15], 0x1400
	s_nop 0
	v_addc_co_u32_e32 v93, vcc, 0, v81, vcc
	global_load_ushort v112, v[92:93], off offset:-4096
	global_load_ushort v107, v[86:87], off offset:2048
	global_load_ushort v172, v[92:93], off
	v_lshl_add_u64 v[86:87], v[82:83], 0, s[14:15]
	v_lshl_add_u64 v[100:101], v[86:87], 2, s[0:1]
	v_lshl_add_u64 v[86:87], v[86:87], 1, s[88:89]
	s_mov_b64 s[14:15], 0x7800
	global_load_dword v100, v[100:101], off
	v_readlane_b32 s50, v254, 23
	global_load_ushort v113, v[86:87], off
	v_lshl_add_u64 v[86:87], v[80:81], 0, s[14:15]
	s_mov_b32 s14, 0x8000
	global_load_ushort v114, v[92:93], off offset:2048
	global_load_ushort v111, v[86:87], off offset:2048
	v_add_co_u32_e32 v86, vcc, s14, v80
	s_mov_b64 s[14:15], 0x9000
	s_nop 0
	v_addc_co_u32_e32 v87, vcc, 0, v81, vcc
	global_load_ushort v173, v[86:87], off offset:2048
	v_lshl_add_u64 v[86:87], v[82:83], 0, s[78:79]
	v_lshl_add_u64 v[92:93], v[86:87], 2, s[0:1]
	v_lshl_add_u64 v[86:87], v[86:87], 1, s[88:89]
	global_load_dword v101, v[92:93], off
	global_load_ushort v176, v[86:87], off
	v_lshl_add_u64 v[86:87], v[80:81], 0, s[14:15]
	s_mov_b32 s14, 0xa000
	v_add_co_u32_e32 v92, vcc, s14, v80
	s_mov_b64 s[14:15], 0x1c00
	s_nop 0
	v_addc_co_u32_e32 v93, vcc, 0, v81, vcc
	v_lshl_add_u64 v[82:83], v[82:83], 0, s[14:15]
	global_load_ushort v177, v[92:93], off offset:-4096
	global_load_ushort v115, v[86:87], off offset:2048
	global_load_ushort v174, v[92:93], off
	v_lshl_add_u64 v[86:87], v[82:83], 2, s[0:1]
	global_load_dword v86, v[86:87], off
	v_lshl_add_u64 v[82:83], v[82:83], 1, s[88:89]
	s_mov_b64 s[14:15], 0xa800
	global_load_ushort v186, v[82:83], off
	v_lshl_add_u64 v[82:83], v[80:81], 0, s[14:15]
	s_mov_b32 s14, 0xb000
	v_add_co_u32_e32 v80, vcc, s14, v80
	v_readlane_b32 s51, v254, 24
	s_nop 0
	v_addc_co_u32_e32 v81, vcc, 0, v81, vcc
	global_load_ushort v188, v[92:93], off offset:2048
	global_load_ushort v182, v[82:83], off offset:2048
	global_load_ushort v175, v[80:81], off offset:2048
	v_readlane_b32 s52, v254, 25
	v_readlane_b32 s53, v254, 26
	global_load_dword v88, v68, s[50:51]
	s_nop 3
	global_load_dword v230, v68, s[56:57]
	global_load_dword v68, v68, s[52:53]
	s_waitcnt vmcnt(0)
; __device__ __forceinline__ float quadsum(float x) { x += dpp_f(x, 0); x += dpp_f(x, 1); return x; }
; __device__ __forceinline__ void p4a_chunk(Frame& F0, const In& I) {
;     ...
;         for (int i = 0; i < 8; ++i) { const size_t tok = tok0 + i; lwv[i] = LW[tok * RW + hc]; ic[i] = bf2f(ICL[tok * RW + hc]);
;             rr[i] = bf2f(RKV[tok * (3 * RW) + hc]); kk[i] = bf2f(RKV[tok * (3 * RW) + RW + hc]); vv[i] = bf2f(RKV[tok * (3 * RW) + 2 * RW + hc]); }
;         const float kkp = I.k_k[hc], kap = I.k_a[hc];
; __device__ __forceinline__ void p5_post(Frame& F0, const In& I) {
;     ...
;         for (int e = 0; e < 16; ++e) { s += y[e]; const float kp = kk[e] * (1.0f + (ic[e] - 1.0f) * p_ka[e]); bs += rr[e] * kp * p_rk[e]; }
;         s = quadsum(s); bs = quadsum(bs);
	v_lshlrev_b32_e32 v231, 16, v84
	v_lshlrev_b32_e32 v232, 16, v85
	v_lshlrev_b32_e32 v233, 16, v90
	v_add_f32_e32 v231, -1.0, v231
	v_fma_f32 v231, v231, v68, 1.0
	v_mul_f32_e32 v232, v232, v231
	v_mul_f32_e32 v233, v233, v232
	v_mul_f32_e32 v234, v233, v230
	v_lshlrev_b32_e32 v231, 16, v95
	v_lshlrev_b32_e32 v232, 16, v91
	v_lshlrev_b32_e32 v233, 16, v96
	v_add_f32_e32 v231, -1.0, v231
	v_fma_f32 v231, v231, v68, 1.0
	v_mul_f32_e32 v232, v232, v231
	v_mul_f32_e32 v233, v233, v232
	v_mul_f32_e32 v235, v233, v230
	v_lshlrev_b32_e32 v231, 16, v97
	v_lshlrev_b32_e32 v232, 16, v98
	v_lshlrev_b32_e32 v233, 16, v99
	v_add_f32_e32 v231, -1.0, v231
	v_fma_f32 v231, v231, v68, 1.0
	v_mul_f32_e32 v232, v232, v231
	v_mul_f32_e32 v233, v233, v232
	v_mul_f32_e32 v236, v233, v230
	v_lshlrev_b32_e32 v231, 16, v102
	v_lshlrev_b32_e32 v232, 16, v103
	v_lshlrev_b32_e32 v233, 16, v106
	v_add_f32_e32 v231, -1.0, v231
	v_fma_f32 v231, v231, v68, 1.0
	v_mul_f32_e32 v232, v232, v231
	v_mul_f32_e32 v233, v233, v232
	v_mul_f32_e32 v237, v233, v230
	v_lshlrev_b32_e32 v231, 16, v110
	v_lshlrev_b32_e32 v232, 16, v107
	v_lshlrev_b32_e32 v233, 16, v112
	v_add_f32_e32 v231, -1.0, v231
	v_fma_f32 v231, v231, v68, 1.0
	v_mul_f32_e32 v232, v232, v231
	v_mul_f32_e32 v233, v233, v232
	v_mul_f32_e32 v238, v233, v230
	v_lshlrev_b32_e32 v231, 16, v113
	v_lshlrev_b32_e32 v232, 16, v111
	v_lshlrev_b32_e32 v233, 16, v114
	v_add_f32_e32 v231, -1.0, v231
	v_fma_f32 v231, v231, v68, 1.0
	v_mul_f32_e32 v232, v232, v231
	v_mul_f32_e32 v233, v233, v232
	v_mul_f32_e32 v239, v233, v230
	v_lshlrev_b32_e32 v231, 16, v176
	v_lshlrev_b32_e32 v232, 16, v115
	v_lshlrev_b32_e32 v233, 16, v177
	v_add_f32_e32 v231, -1.0, v231
	v_fma_f32 v231, v231, v68, 1.0
	v_mul_f32_e32 v232, v232, v231
	v_mul_f32_e32 v233, v233, v232
	v_mul_f32_e32 v240, v233, v230
	v_lshlrev_b32_e32 v231, 16, v186
	v_lshlrev_b32_e32 v232, 16, v182
	v_lshlrev_b32_e32 v233, 16, v188
	v_add_f32_e32 v231, -1.0, v231
	v_fma_f32 v231, v231, v68, 1.0
	v_mul_f32_e32 v232, v232, v231
	v_mul_f32_e32 v233, v233, v232
	v_mul_f32_e32 v241, v233, v230
	v_add_f32_dpp v234, v234, v234 quad_perm:[1,0,3,2] row_mask:0xf bank_mask:0xf bound_ctrl:1
	v_add_f32_dpp v235, v235, v235 quad_perm:[1,0,3,2] row_mask:0xf bank_mask:0xf bound_ctrl:1
	v_add_f32_dpp v236, v236, v236 quad_perm:[1,0,3,2] row_mask:0xf bank_mask:0xf bound_ctrl:1
	v_add_f32_dpp v237, v237, v237 quad_perm:[1,0,3,2] row_mask:0xf bank_mask:0xf bound_ctrl:1
	v_add_f32_dpp v238, v238, v238 quad_perm:[1,0,3,2] row_mask:0xf bank_mask:0xf bound_ctrl:1
	v_add_f32_dpp v239, v239, v239 quad_perm:[1,0,3,2] row_mask:0xf bank_mask:0xf bound_ctrl:1
	v_add_f32_dpp v240, v240, v240 quad_perm:[1,0,3,2] row_mask:0xf bank_mask:0xf bound_ctrl:1
	v_add_f32_dpp v241, v241, v241 quad_perm:[1,0,3,2] row_mask:0xf bank_mask:0xf bound_ctrl:1
	v_add_f32_dpp v234, v234, v234 quad_perm:[2,3,0,1] row_mask:0xf bank_mask:0xf bound_ctrl:1
	v_add_f32_dpp v235, v235, v235 quad_perm:[2,3,0,1] row_mask:0xf bank_mask:0xf bound_ctrl:1
	v_add_f32_dpp v236, v236, v236 quad_perm:[2,3,0,1] row_mask:0xf bank_mask:0xf bound_ctrl:1
	v_add_f32_dpp v237, v237, v237 quad_perm:[2,3,0,1] row_mask:0xf bank_mask:0xf bound_ctrl:1
	v_add_f32_dpp v238, v238, v238 quad_perm:[2,3,0,1] row_mask:0xf bank_mask:0xf bound_ctrl:1
	v_add_f32_dpp v239, v239, v239 quad_perm:[2,3,0,1] row_mask:0xf bank_mask:0xf bound_ctrl:1
	v_add_f32_dpp v240, v240, v240 quad_perm:[2,3,0,1] row_mask:0xf bank_mask:0xf bound_ctrl:1
	v_add_f32_dpp v241, v241, v241 quad_perm:[2,3,0,1] row_mask:0xf bank_mask:0xf bound_ctrl:1
	v_add_f32_dpp v234, v234, v234 row_ror:4 row_mask:0xf bank_mask:0xf bound_ctrl:1
	v_add_f32_dpp v235, v235, v235 row_ror:4 row_mask:0xf bank_mask:0xf bound_ctrl:1
	v_add_f32_dpp v236, v236, v236 row_ror:4 row_mask:0xf bank_mask:0xf bound_ctrl:1
	v_add_f32_dpp v237, v237, v237 row_ror:4 row_mask:0xf bank_mask:0xf bound_ctrl:1
	v_add_f32_dpp v238, v238, v238 row_ror:4 row_mask:0xf bank_mask:0xf bound_ctrl:1
	v_add_f32_dpp v239, v239, v239 row_ror:4 row_mask:0xf bank_mask:0xf bound_ctrl:1
	v_add_f32_dpp v240, v240, v240 row_ror:4 row_mask:0xf bank_mask:0xf bound_ctrl:1
	v_add_f32_dpp v241, v241, v241 row_ror:4 row_mask:0xf bank_mask:0xf bound_ctrl:1
	v_add_f32_dpp v234, v234, v234 row_ror:8 row_mask:0xf bank_mask:0xf bound_ctrl:1
	v_add_f32_dpp v235, v235, v235 row_ror:8 row_mask:0xf bank_mask:0xf bound_ctrl:1
	v_add_f32_dpp v236, v236, v236 row_ror:8 row_mask:0xf bank_mask:0xf bound_ctrl:1
; #define LAS __attribute__((address_space(3)))
; #define CBAR() do { asm volatile("s_waitcnt lgkmcnt(0)" ::: "memory"); __builtin_amdgcn_s_barrier(); asm volatile("" ::: "memory"); } while (0)
; __device__ __forceinline__ float rowsum16(float x) { x += dpp_f(x, 0); x += dpp_f(x, 1); x += dpp_f(x, 2); x += dpp_f(x, 3); return x; }
; __device__ __forceinline__ float quadsum(float x) { x += dpp_f(x, 0); x += dpp_f(x, 1); return x; }
; __device__ __forceinline__ float wave_sum(float v) {
;     v = rowsum16(v);
;     const int vi = __builtin_bit_cast(int, v);
;     const float s0 = __builtin_bit_cast(float, __builtin_amdgcn_readlane(vi, 0)), s1 = __builtin_bit_cast(float, __builtin_amdgcn_readlane(vi, 16));
;     const float s2 = __builtin_bit_cast(float, __builtin_amdgcn_readlane(vi, 32)), s3 = __builtin_bit_cast(float, __builtin_amdgcn_readlane(vi, 48));
;     return (s0 + s1) + (s2 + s3);
; __device__ __forceinline__ void p4a_chunk(Frame& F0, const In& I) {
;     ...
;         float cs[8]; { float run = 0.f;
; #pragma unroll
;             for (int i = 0; i < 8; ++i) { run += lwv[i]; cs[i] = run; } }
;         __syncthreads();
;         ((LAS float*)(L + C_SEG))[w * 64 + lane] = cs[7];
;         CBAR();
;         float pre = 0.f, tot = 0.f;
; #pragma unroll
;         for (int j = 0; j < 8; ++j) { const float sg = ((const LAS float*)(L + C_SEG))[j * 64 + lane]; tot += sg; pre += (j < w) ? sg : 0.f; }
;         if (w == 0) ((LAS float*)(L + C_GAM))[lane] = __expf(tot);
	v_add_f32_dpp v237, v237, v237 row_ror:8 row_mask:0xf bank_mask:0xf bound_ctrl:1
	v_add_f32_dpp v238, v238, v238 row_ror:8 row_mask:0xf bank_mask:0xf bound_ctrl:1
	v_add_f32_dpp v239, v239, v239 row_ror:8 row_mask:0xf bank_mask:0xf bound_ctrl:1
	v_add_f32_dpp v240, v240, v240 row_ror:8 row_mask:0xf bank_mask:0xf bound_ctrl:1
	v_add_f32_dpp v241, v241, v241 row_ror:8 row_mask:0xf bank_mask:0xf bound_ctrl:1
	v_readlane_b32 s58, v234, 16
	v_readlane_b32 s59, v234, 32
	v_readlane_b32 s60, v234, 48
	s_nop 1
	v_add_f32_e32 v234, s58, v234
	v_add_f32_e32 v234, s59, v234
	v_add_f32_e32 v234, s60, v234
	v_readlane_b32 s58, v235, 16
	v_readlane_b32 s59, v235, 32
	v_readlane_b32 s60, v235, 48
	s_nop 1
	v_add_f32_e32 v235, s58, v235
	v_add_f32_e32 v235, s59, v235
	v_add_f32_e32 v235, s60, v235
	v_readlane_b32 s58, v236, 16
	v_readlane_b32 s59, v236, 32
	v_readlane_b32 s60, v236, 48
	s_nop 1
	v_add_f32_e32 v236, s58, v236
	v_add_f32_e32 v236, s59, v236
	v_add_f32_e32 v236, s60, v236
	v_readlane_b32 s58, v237, 16
	v_readlane_b32 s59, v237, 32
	v_readlane_b32 s60, v237, 48
	s_nop 1
	v_add_f32_e32 v237, s58, v237
	v_add_f32_e32 v237, s59, v237
	v_add_f32_e32 v237, s60, v237
	v_readlane_b32 s58, v238, 16
	v_readlane_b32 s59, v238, 32
	v_readlane_b32 s60, v238, 48
	s_nop 1
	v_add_f32_e32 v238, s58, v238
	v_add_f32_e32 v238, s59, v238
	v_add_f32_e32 v238, s60, v238
	v_readlane_b32 s58, v239, 16
	v_readlane_b32 s59, v239, 32
	v_readlane_b32 s60, v239, 48
	s_nop 1
	v_add_f32_e32 v239, s58, v239
	v_add_f32_e32 v239, s59, v239
	v_add_f32_e32 v239, s60, v239
	v_readlane_b32 s58, v240, 16
	v_readlane_b32 s59, v240, 32
	v_readlane_b32 s60, v240, 48
	s_nop 1
	v_add_f32_e32 v240, s58, v240
	v_add_f32_e32 v240, s59, v240
	v_add_f32_e32 v240, s60, v240
	v_readlane_b32 s58, v241, 16
	v_readlane_b32 s59, v241, 32
	v_readlane_b32 s60, v241, 48
	s_nop 1
	v_add_f32_e32 v241, s58, v241
	v_add_f32_e32 v241, s59, v241
	v_add_f32_e32 v241, s60, v241
	v_mov_b32_e32 v242, 0
	v_cmp_eq_u32_e32 vcc, 0, v1
	s_nop 1
	v_cndmask_b32_e32 v242, v242, v234, vcc
	v_cmp_eq_u32_e32 vcc, 1, v1
	s_nop 1
	v_cndmask_b32_e32 v242, v242, v235, vcc
	v_cmp_eq_u32_e32 vcc, 2, v1
	s_nop 1
	v_cndmask_b32_e32 v242, v242, v236, vcc
	v_cmp_eq_u32_e32 vcc, 3, v1
	s_nop 1
	v_cndmask_b32_e32 v242, v242, v237, vcc
	v_cmp_eq_u32_e32 vcc, 4, v1
	s_nop 1
	v_cndmask_b32_e32 v242, v242, v238, vcc
	v_cmp_eq_u32_e32 vcc, 5, v1
	s_nop 1
	v_cndmask_b32_e32 v242, v242, v239, vcc
	v_cmp_eq_u32_e32 vcc, 6, v1
	s_nop 1
	v_cndmask_b32_e32 v242, v242, v240, vcc
	v_cmp_eq_u32_e32 vcc, 7, v1
	s_nop 1
	v_cndmask_b32_e32 v242, v242, v241, vcc
	s_ashr_i32 s48, s13, 11
	s_lshl_b32 s48, s48, 13
	s_lshl_b32 s49, s13, 6
	s_and_b32 s49, s49, 0x1fc0
	s_add_i32 s49, s49, s22
	s_add_i32 s48, s48, s49
	s_lshl_b32 s48, s48, 6
	s_lshr_b32 s49, s13, 5
	s_and_b32 s49, s49, 0x3c
	s_add_i32 s48, s48, s49
	v_lshl_add_u32 v243, v1, 6, s48
	s_add_u32 s50, s96, 0x1c00000
	s_addc_u32 s51, s97, 0
	s_mov_b64 s[62:63], exec
	s_mov_b64 exec, 0xff
	global_store_dword v243, v242, s[50:51]
	s_mov_b64 exec, s[62:63]
	s_waitcnt vmcnt(41)
	v_add_f32_e32 v187, 0, v89
	s_waitcnt vmcnt(36)
	v_add_f32_e32 v185, v187, v94
	s_waitcnt vmcnt(31)
	v_add_f32_e32 v184, v185, v104
	s_barrier
	s_andn2_b64 vcc, exec, s[24:25]
	v_readlane_b32 s49, v254, 22
	s_waitcnt vmcnt(26)
	v_add_f32_e32 v183, v184, v105
	v_readlane_b32 s54, v254, 27
	v_readlane_b32 s55, v254, 28
	v_readlane_b32 s56, v254, 29
	v_readlane_b32 s57, v254, 30
	v_readlane_b32 s58, v254, 31
	v_readlane_b32 s59, v254, 32
	v_readlane_b32 s60, v254, 33
	v_readlane_b32 s61, v254, 34
	v_readlane_b32 s62, v254, 35
	v_readlane_b32 s63, v254, 36
	s_waitcnt vmcnt(21)
	v_add_f32_e32 v181, v183, v108
	s_waitcnt vmcnt(16)
	v_add_f32_e32 v180, v181, v100
	s_waitcnt vmcnt(11)
	v_add_f32_e32 v179, v180, v101
	s_waitcnt vmcnt(6)
	v_add_f32_e32 v178, v179, v86
	ds_write_b32 v117, v178
	s_waitcnt lgkmcnt(0)
	s_barrier
	ds_read2st64_b32 v[82:83], v118 offset1:1
	ds_read2st64_b32 v[86:87], v118 offset0:2 offset1:3
	ds_read2st64_b32 v[92:93], v118 offset0:4 offset1:5
	ds_read2st64_b32 v[100:101], v118 offset0:6 offset1:7
	s_waitcnt lgkmcnt(3)
	v_add_f32_e32 v82, 0, v82
	v_add_f32_e32 v80, v82, v83
	s_waitcnt lgkmcnt(2)
	v_add_f32_e32 v80, v80, v86
	v_add_f32_e32 v80, v80, v87
	s_waitcnt lgkmcnt(1)
	v_add_f32_e32 v80, v80, v92
	v_add_f32_e32 v80, v80, v93
	s_waitcnt lgkmcnt(0)
	v_add_f32_e32 v80, v80, v100
	v_add_f32_e32 v80, v80, v101
	v_mul_f32_e32 v80, 0x3fb8aa3b, v80
	v_exp_f32_e32 v94, v80
	s_cbranch_vccnz .LBB0_1085
	ds_write_b32 v119, v94

; #define GAS __attribute__((address_space(1)))
; __device__ __forceinline__ void p5_post(Frame& F0, const In& I) {
;     ...
;     for (int q = 0; q < 4; ++q) { const f32x4 a = *(const GAS f32x4*)(I.k_a + c0 + 4 * q), bq = *(const GAS f32x4*)(I.r_k + c0 + 4 * q), c = *(const GAS f32x4*)(I.lnx_w + c0 + 4 * q), d = *(const GAS f32x4*)(I.lnx_b + c0 + 4 * q);
; #pragma unroll
;         for (int e = 0; e < 4; ++e) { p_ka[4 * q + e] = a[e]; p_rk[4 * q + e] = bq[e]; p_lw[4 * q + e] = c[e]; p_lb[4 * q + e] = d[e]; } }
;     v4u raw[12];
;     ...
;     if (gw < T) P5_LOAD(gw);
.LBB0_1211:
	s_or_b64 exec, exec, s[0:1]
	s_waitcnt lgkmcnt(0)
	v_mov_b32_e32 v1, v0
	s_barrier
	v_readlane_b32 s1, v254, 53
	v_readfirstlane_b32 s0, v1
	s_ashr_i32 s0, s0, 6
	s_add_i32 s2, s0, s1
	s_cmpk_gt_i32 s2, 0x7fff
	s_cbranch_scc1 .LBB0_1216
	s_ashr_i32 s3, s2, 31
	s_lshl_b64 s[6:7], s[2:3], 11
	s_add_u32 s4, s96, s6
	s_addc_u32 s5, s97, s7
	v_lshlrev_b32_e32 v2, 4, v1
	s_add_u32 s8, s88, s6
	v_and_b32_e32 v68, 0x3f0, v2
	v_mov_b32_e32 v162, 0
	s_addc_u32 s9, s89, s7
	s_mul_i32 s3, s2, 0x1800
	v_readlane_b32 s10, v254, 54
	v_lshlrev_b32_e32 v58, 1, v68
	v_mov_b32_e32 v59, v162
	s_mul_hi_i32 s1, s2, 0x1800
	v_readlane_b32 s11, v254, 55
	s_add_u32 s10, s10, s3
	v_lshl_add_u64 v[60:61], s[4:5], 0, v[58:59]
	s_mov_b64 s[4:5], 0x90000000
	s_addc_u32 s11, s11, s1
	s_brev_b32 s1, 9
	v_readlane_b32 s12, v254, 21
	v_lshl_add_u64 v[62:63], v[60:61], 0, s[4:5]
	v_add_co_u32_e32 v60, vcc, s1, v60
	v_lshlrev_b32_e32 v69, 2, v68
	v_readlane_b32 s16, v254, 25
	v_readlane_b32 s17, v254, 26
	v_lshl_add_u64 v[64:65], s[10:11], 0, v[58:59]
	v_addc_co_u32_e32 v61, vcc, 0, v61, vcc
	s_movk_i32 s1, 0x1000
	v_readlane_b32 s13, v254, 22
	v_readlane_b32 s18, v254, 27
	v_readlane_b32 s19, v254, 28
	v_readlane_b32 s20, v254, 29
	v_readlane_b32 s21, v254, 30
	v_readlane_b32 s22, v254, 31
	v_readlane_b32 s23, v254, 32
	global_load_dwordx4 v[2:5], v69, s[16:17]
	global_load_dwordx4 v[6:9], v69, s[18:19]
	global_load_dwordx4 v[10:13], v69, s[16:17] offset:16
	global_load_dwordx4 v[14:17], v69, s[18:19] offset:16
	global_load_dwordx4 v[18:21], v69, s[16:17] offset:32
	global_load_dwordx4 v[22:25], v69, s[18:19] offset:32
	global_load_dwordx4 v[26:29], v69, s[20:21]
	global_load_dwordx4 v[30:33], v69, s[22:23]
	global_load_dwordx4 v[34:37], v69, s[20:21] offset:16
	global_load_dwordx4 v[38:41], v69, s[22:23] offset:16
	global_load_dwordx4 v[42:45], v69, s[20:21] offset:32
	global_load_dwordx4 v[46:49], v69, s[22:23] offset:32
	global_load_dwordx4 v[50:53], v69, s[20:21] offset:48
	global_load_dwordx4 v[54:57], v69, s[22:23] offset:48
	s_add_u32 s100, s96, 0x1c00000
	s_addc_u32 s101, s97, 0
	s_lshl_b32 s98, s2, 6
	s_add_u32 s98, s100, s98
	s_addc_u32 s99, s101, 0
	v_and_b32_e32 v241, 60, v0
	global_load_dword v242, v241, s[98:99]
	global_load_dwordx4 v[134:137], v[60:61], off
	global_load_dwordx4 v[114:117], v[62:63], off offset:16
	v_add_co_u32_e32 v60, vcc, s1, v64
	s_mov_b64 s[12:13], 0x1000
	s_add_u32 s6, s66, s6
	v_addc_co_u32_e32 v61, vcc, 0, v65, vcc
	v_lshl_add_u64 v[66:67], v[64:65], 0, s[12:13]
	s_addc_u32 s7, s67, s7
	global_load_dwordx4 v[154:157], v[60:61], off
	global_load_dwordx4 v[130:133], v[66:67], off offset:16
	global_load_dwordx4 v[138:141], v58, s[6:7] offset:16
	global_load_dwordx4 v[158:161], v58, s[6:7]
	s_nop 0
	global_load_dwordx4 v[58:61], v69, s[18:19] offset:48
	global_load_dwordx4 v[62:65], v69, s[16:17] offset:48
	v_readlane_b32 s6, v254, 53
	s_ashr_i32 s1, s0, 31
	s_ashr_i32 s3, s6, 31
	s_add_u32 s0, s0, s6
	s_addc_u32 s1, s1, s3
	s_add_i32 s12, s2, s68
	s_lshl_b64 s[0:1], s[0:1], 10
	s_mov_b64 s[8:9], 0x98000000
	v_lshlrev_b32_e32 v1, 5, v1
	s_ashr_i32 s13, s12, 31
	v_or_b32_e32 v66, s0, v68
	v_mov_b32_e32 v67, s1
	v_readlane_b32 s14, v254, 23
	v_readlane_b32 s15, v254, 24
	v_and_b32_e32 v1, 0x7e0, v1
	s_ashr_i32 s69, s68, 31
	s_mul_hi_i32 s3, s12, 0x1800
	s_mul_i32 s10, s12, 0x1800
	v_lshl_add_u64 v[166:167], v[66:67], 0, s[8:9]
	s_lshl_b64 s[0:1], s[12:13], 11
	s_lshl_b64 s[6:7], s[68:69], 10
	v_or_b32_e32 v164, s10, v1
	v_mov_b32_e32 v165, s3
	s_mul_hi_i32 s11, s68, 0x1800
	s_mul_i32 s10, s68, 0x1800
	v_or_b32_e32 v170, s0, v1
	v_mov_b32_e32 v171, s1
	s_lshl_b64 s[12:13], s[68:69], 11
	s_mov_b64 s[14:15], 0x84000000
	s_mov_b64 s[16:17], 0x6e000000
	s_mov_b64 s[18:19], 0x6e000800
	s_mov_b64 s[20:21], 0x6e001000
	s_mov_b64 s[22:23], 0x8c000000
	s_mov_b32 s3, 0x6e001000
	v_mov_b32_e32 v1, 0x3a27c5ac
	s_mov_b32 s8, 0xf800000
	v_mov_b32_e32 v173, 0x3c800000
	v_readlane_b32 s24, v254, 33
	v_readlane_b32 s25, v254, 34
	v_readlane_b32 s26, v254, 35
	v_readlane_b32 s27, v254, 36
	s_waitcnt vmcnt(0)
	v_mov_b64_e32 v[66:67], v[134:135]
	s_waitcnt vmcnt(12)
	v_mov_b64_e32 v[70:71], v[114:115]
	s_waitcnt vmcnt(11)
	v_mov_b64_e32 v[78:79], v[118:119]
	s_waitcnt vmcnt(10)
	v_mov_b64_e32 v[74:75], v[142:143]
	s_waitcnt vmcnt(9)
	v_mov_b64_e32 v[86:87], v[122:123]
	s_waitcnt vmcnt(8)
	v_mov_b64_e32 v[82:83], v[146:147]
	s_waitcnt vmcnt(7)
	v_mov_b64_e32 v[94:95], v[126:127]
	s_waitcnt vmcnt(6)
	v_mov_b64_e32 v[90:91], v[150:151]
	v_mov_b32_e32 v169, v52
	v_mov_b32_e32 v52, 0x260
	v_mov_b64_e32 v[68:69], v[136:137]
	s_waitcnt vmcnt(5)
	v_mov_b64_e32 v[98:99], v[154:155]
	s_waitcnt vmcnt(4)
	v_mov_b64_e32 v[102:103], v[130:131]
	s_waitcnt vmcnt(3)
	v_mov_b64_e32 v[110:111], v[138:139]
	s_waitcnt vmcnt(2)
	v_mov_b64_e32 v[106:107], v[158:159]
	v_mov_b64_e32 v[72:73], v[116:117]
	v_mov_b64_e32 v[76:77], v[144:145]
	v_mov_b64_e32 v[80:81], v[120:121]
	v_mov_b64_e32 v[84:85], v[148:149]
	v_mov_b64_e32 v[88:89], v[124:125]
	v_mov_b64_e32 v[92:93], v[152:153]
	v_mov_b64_e32 v[96:97], v[128:129]
	v_mov_b64_e32 v[100:101], v[156:157]
	v_mov_b64_e32 v[104:105], v[132:133]
	v_mov_b64_e32 v[108:109], v[160:161]
	v_mov_b64_e32 v[112:113], v[140:141]
	s_branch .LBB0_1214
; __device__ __forceinline__ void p5_post(Frame& F0, const In& I) {
;     ...
;         float y[16], rr[16], kk[16], vv[16], ic[16], gg[16];
; #pragma unroll
;         for (int q = 0; q < 2; ++q) {
;             const unsigned yw[4] = {raw[q].x, raw[q].y, raw[q].z, raw[q].w}, iw[4] = {raw[2 + q].x, raw[2 + q].y, raw[2 + q].z, raw[2 + q].w};
;             const unsigned aw[4] = {raw[4 + q].x, raw[4 + q].y, raw[4 + q].z, raw[4 + q].w}, bw[4] = {raw[6 + q].x, raw[6 + q].y, raw[6 + q].z, raw[6 + q].w};
;             const unsigned cw[4] = {raw[8 + q].x, raw[8 + q].y, raw[8 + q].z, raw[8 + q].w}, dw[4] = {raw[10 + q].x, raw[10 + q].y, raw[10 + q].z, raw[10 + q].w};
; #pragma unroll
;             for (int e = 0; e < 4; ++e) { y[8 * q + 2 * e] = bflo(yw[e]); y[8 * q + 2 * e + 1] = bfhi(yw[e]); ic[8 * q + 2 * e] = bflo(iw[e]); ic[8 * q + 2 * e + 1] = bfhi(iw[e]);
;                 rr[8 * q + 2 * e] = bflo(aw[e]); rr[8 * q + 2 * e + 1] = bfhi(aw[e]); kk[8 * q + 2 * e] = bflo(bw[e]); kk[8 * q + 2 * e + 1] = bfhi(bw[e]);
;                 vv[8 * q + 2 * e] = bflo(cw[e]); vv[8 * q + 2 * e + 1] = bfhi(cw[e]); gg[8 * q + 2 * e] = bflo(dw[e]); gg[8 * q + 2 * e + 1] = bfhi(dw[e]); } }
;         __builtin_amdgcn_sched_barrier(0);
;         if (tok + NGW < T) P5_LOAD(tok + NGW);
;         __builtin_amdgcn_sched_barrier(0);
;         float s = 0.f, bs = 0.f;
; #pragma unroll
;         for (int e = 0; e < 16; ++e) { s += y[e]; const float kp = kk[e] * (1.0f + (ic[e] - 1.0f) * p_ka[e]); bs += rr[e] * kp * p_rk[e]; }
.LBB0_1213:
	v_lshlrev_b32_e32 v198, 16, v134
	v_lshlrev_b32_e32 v172, 16, v142
	v_and_b32_e32 v176, 0xffff0000, v142
	v_lshlrev_b32_e32 v190, 16, v146
	v_and_b32_e32 v175, 0xffff0000, v134
	v_and_b32_e32 v178, 0xffff0000, v146
	v_lshlrev_b32_e32 v180, 16, v150
	v_and_b32_e32 v182, 0xffff0000, v150
	v_lshlrev_b32_e32 v174, 16, v154
	v_and_b32_e32 v150, 0xffff0000, v154
	v_lshlrev_b32_e32 v177, 16, v135
	v_and_b32_e32 v163, 0xffff0000, v135
	v_lshlrev_b32_e32 v135, 16, v143
	v_and_b32_e32 v143, 0xffff0000, v143
	v_lshlrev_b32_e32 v192, 16, v147
	v_and_b32_e32 v147, 0xffff0000, v147
	v_lshlrev_b32_e32 v201, 16, v151
	v_and_b32_e32 v151, 0xffff0000, v151
	v_lshlrev_b32_e32 v154, 16, v155
	v_and_b32_e32 v146, 0xffff0000, v155
	v_lshlrev_b32_e32 v202, 16, v159
	v_and_b32_e32 v203, 0xffff0000, v159
	v_lshlrev_b32_e32 v159, 16, v136
	v_and_b32_e32 v179, 0xffff0000, v136
	v_lshlrev_b32_e32 v155, 16, v144
	v_and_b32_e32 v204, 0xffff0000, v144
	v_lshlrev_b32_e32 v205, 16, v148
	v_and_b32_e32 v206, 0xffff0000, v148
	v_lshlrev_b32_e32 v207, 16, v152
	v_and_b32_e32 v152, 0xffff0000, v152
	v_lshlrev_b32_e32 v148, 16, v156
	v_and_b32_e32 v142, 0xffff0000, v156
	v_lshlrev_b32_e32 v208, 16, v160
	v_and_b32_e32 v209, 0xffff0000, v160
	v_lshlrev_b32_e32 v181, 16, v137
	v_and_b32_e32 v183, 0xffff0000, v137
	v_lshlrev_b32_e32 v137, 16, v145
	v_and_b32_e32 v145, 0xffff0000, v145
	v_lshlrev_b32_e32 v156, 16, v149
	v_and_b32_e32 v149, 0xffff0000, v149
	v_lshlrev_b32_e32 v160, 16, v153
	v_and_b32_e32 v210, 0xffff0000, v153
	v_lshlrev_b32_e32 v144, 16, v157
	v_and_b32_e32 v134, 0xffff0000, v157
	v_lshlrev_b32_e32 v211, 16, v161
	v_and_b32_e32 v212, 0xffff0000, v161
	v_lshlrev_b32_e32 v153, 16, v114
	v_and_b32_e32 v157, 0xffff0000, v114
	v_lshlrev_b32_e32 v213, 16, v118
	v_and_b32_e32 v214, 0xffff0000, v118
	v_lshlrev_b32_e32 v215, 16, v122
	v_and_b32_e32 v216, 0xffff0000, v122
	v_lshlrev_b32_e32 v217, 16, v126
	v_and_b32_e32 v218, 0xffff0000, v126
	v_lshlrev_b32_e32 v136, 16, v130
	v_and_b32_e32 v126, 0xffff0000, v130
	v_lshlrev_b32_e32 v219, 16, v138
	v_and_b32_e32 v220, 0xffff0000, v138
	v_lshlrev_b32_e32 v161, 16, v115
	v_lshlrev_b32_e32 v138, 16, v119
	v_and_b32_e32 v119, 0xffff0000, v119
	v_lshlrev_b32_e32 v221, 16, v123
	v_and_b32_e32 v123, 0xffff0000, v123
	v_lshlrev_b32_e32 v222, 16, v127
	v_and_b32_e32 v127, 0xffff0000, v127
	v_lshlrev_b32_e32 v122, 16, v131
	v_and_b32_e32 v114, 0xffff0000, v131
	v_lshlrev_b32_e32 v223, 16, v139
	v_and_b32_e32 v224, 0xffff0000, v139
	v_lshlrev_b32_e32 v131, 16, v116
	v_and_b32_e32 v130, 0xffff0000, v115
	v_and_b32_e32 v139, 0xffff0000, v116
	v_and_b32_e32 v185, 0xffff0000, v120
	v_lshlrev_b32_e32 v184, 16, v120
	v_and_b32_e32 v187, 0xffff0000, v124
	v_lshlrev_b32_e32 v186, 16, v124
	v_lshlrev_b32_e32 v120, 16, v132
	v_and_b32_e32 v116, 0xffff0000, v132
	v_and_b32_e32 v197, 0xffff0000, v125
	v_lshlrev_b32_e32 v196, 16, v125
	v_and_b32_e32 v125, 0xffff0000, v129
	v_lshlrev_b32_e32 v124, 16, v129
	v_and_b32_e32 v118, 0xffff0000, v133
	v_lshlrev_b32_e32 v199, 16, v158
	v_and_b32_e32 v200, 0xffff0000, v158
	v_and_b32_e32 v189, 0xffff0000, v128
	v_lshlrev_b32_e32 v188, 16, v128
	v_lshlrev_b32_e32 v225, 16, v140
	v_and_b32_e32 v226, 0xffff0000, v140
	v_lshlrev_b32_e32 v191, 16, v117
	v_and_b32_e32 v193, 0xffff0000, v117
	v_and_b32_e32 v195, 0xffff0000, v121
	v_lshlrev_b32_e32 v194, 16, v121
	v_lshlrev_b32_e32 v168, 16, v133
	v_lshlrev_b32_e32 v227, 16, v141
	v_and_b32_e32 v228, 0xffff0000, v141
	v_add_f32_e32 v121, -1.0, v176
	v_fma_f32 v121, v3, v121, 1.0
	v_mul_f32_e32 v121, v121, v182
	v_mul_f32_e32 v121, v121, v178
	v_mul_f32_e32 v158, v7, v121
	v_add_f32_e32 v121, -1.0, v135
	v_fma_f32 v121, v4, v121, 1.0
	v_mul_f32_e32 v121, v121, v201
	v_mul_f32_e32 v121, v121, v192
	v_mul_f32_e32 v178, v8, v121
	v_add_f32_e32 v121, -1.0, v143
	v_fma_f32 v121, v5, v121, 1.0
	v_add_f32_e32 v117, -1.0, v172
	v_mul_f32_e32 v121, v121, v151
	v_fma_f32 v117, v2, v117, 1.0
	v_mul_f32_e32 v121, v121, v147
	v_mul_f32_e32 v117, v117, v180
	v_mul_f32_e32 v180, v9, v121
	v_add_f32_e32 v121, -1.0, v155
	v_fma_f32 v121, v10, v121, 1.0
	v_mul_f32_e32 v121, v121, v207
	v_mul_f32_e32 v121, v121, v205
	v_add_f32_e32 v115, 0, v198
	v_mul_f32_e32 v182, v14, v121
	v_add_f32_e32 v121, -1.0, v204
	v_fma_f32 v121, v11, v121, 1.0
	v_add_f32_e32 v115, v115, v175
	v_mov_b32_e32 v176, v6
	v_mul_f32_e32 v121, v121, v152
	v_pk_add_f32 v[132:133], v[176:177], v[114:115]
	v_add_f32_e32 v115, -1.0, v145
	v_mul_f32_e32 v121, v121, v206
	v_fma_f32 v115, v13, v115, 1.0
	v_mul_f32_e32 v152, v15, v121
	v_add_f32_e32 v121, -1.0, v137
	v_mul_f32_e32 v115, v115, v210
	v_fma_f32 v121, v12, v121, 1.0
	v_mul_f32_e32 v115, v115, v149
	v_mul_f32_e32 v121, v121, v160
	v_mul_f32_e32 v160, v17, v115
	v_add_f32_e32 v115, -1.0, v213
	v_fma_f32 v115, v18, v115, 1.0
	v_mul_f32_e32 v115, v115, v217
	v_mul_f32_e32 v128, v117, v190
	v_mul_f32_e32 v115, v115, v215
	v_pk_mul_f32 v[128:129], v[6:7], v[128:129]
	v_mul_f32_e32 v132, v22, v115
	v_add_f32_e32 v115, -1.0, v214
	v_mov_b32_e32 v129, v133
	v_fma_f32 v115, v19, v115, 1.0
	v_pk_add_f32 v[128:129], v[128:129], v[162:163]
	v_mul_f32_e32 v115, v115, v218
	v_pk_add_f32 v[128:129], v[128:129], v[158:159]
	v_mul_f32_e32 v115, v115, v216
	v_pk_add_f32 v[128:129], v[128:129], v[178:179]
	v_mul_f32_e32 v140, v23, v115
	v_add_f32_e32 v115, -1.0, v138
	v_pk_add_f32 v[128:129], v[128:129], v[180:181]
	v_fma_f32 v115, v20, v115, 1.0
	v_mul_f32_e32 v121, v121, v156
	v_pk_add_f32 v[128:129], v[128:129], v[182:183]
	v_mul_f32_e32 v115, v115, v222
	v_mul_f32_e32 v156, v16, v121
	v_mul_f32_e32 v115, v115, v221
	v_pk_add_f32 v[128:129], v[128:129], v[152:153]
	v_mul_f32_e32 v138, v24, v115
	v_add_f32_e32 v115, -1.0, v119
	v_pk_add_f32 v[184:185], v[184:185], -1.0 op_sel_hi:[1,0]
	v_pk_add_f32 v[128:129], v[128:129], v[156:157]
	v_fma_f32 v115, v21, v115, 1.0
	s_waitcnt vmcnt(0)
; __device__ __forceinline__ float quadsum(float x) { x += dpp_f(x, 0); x += dpp_f(x, 1); return x; }
; __device__ __forceinline__ void p5_post(Frame& F0, const In& I) {
;     ...
;         for (int e = 0; e < 16; ++e) { s += y[e]; const float kp = kk[e] * (1.0f + (ic[e] - 1.0f) * p_ka[e]); bs += rr[e] * kp * p_rk[e]; }
;         s = quadsum(s); bs = quadsum(bs);
;         const float mean = s * (1.f / 64.f); float s2 = 0.f;
; #pragma unroll
;         for (int e = 0; e < 16; ++e) { y[e] -= mean; s2 += y[e] * y[e]; }
;         s2 = quadsum(s2);
;         const float rstd = 1.f / sqrtf(s2 * (1.f / 64.f) + GN_EPS);
;         float o[16];
; #pragma unroll
;         for (int e = 0; e < 16; ++e) o[e] = (y[e] * rstd * p_lw[e] + p_lb[e] + bs * vv[e]) * gg[e];
	v_pk_fma_f32 v[184:185], v[62:63], v[184:185], 1.0 op_sel_hi:[1,1,0]
	v_pk_add_f32 v[128:129], v[128:129], v[160:161]
	v_mov_b32_e32 v133, v130
	v_mul_f32_e32 v115, v115, v127
	v_pk_mul_f32 v[184:185], v[184:185], v[188:189]
	v_pk_add_f32 v[128:129], v[128:129], v[132:133]
	v_mov_b32_e32 v141, v131
	v_mul_f32_e32 v115, v115, v123
	v_pk_mul_f32 v[184:185], v[184:185], v[186:187]
	v_pk_add_f32 v[128:129], v[128:129], v[140:141]
	v_mul_f32_e32 v190, v25, v115
	v_pk_mul_f32 v[184:185], v[58:59], v[184:185]
	v_pk_add_f32 v[186:187], v[194:195], -1.0 op_sel_hi:[1,0]
	v_pk_add_f32 v[128:129], v[128:129], v[138:139]
	v_pk_fma_f32 v[186:187], v[64:65], v[186:187], 1.0 op_sel_hi:[1,1,0]
	v_pk_add_f32 v[128:129], v[128:129], v[190:191]
	v_mov_b32_e32 v192, v184
	v_pk_mul_f32 v[124:125], v[186:187], v[124:125]
	v_pk_add_f32 v[128:129], v[192:193], v[128:129]
	v_mov_b32_e32 v133, v162
	v_pk_mul_f32 v[124:125], v[124:125], v[196:197]
	v_mov_b32_e32 v132, v185
	v_mov_b32_dpp v133, v129 quad_perm:[1,0,3,2] row_mask:0xf bank_mask:0xf
	v_pk_mul_f32 v[124:125], v[60:61], v[124:125]
	v_pk_add_f32 v[128:129], v[132:133], v[128:129]
	v_mov_b32_e32 v133, v162
	v_mov_b32_e32 v132, v124
	v_mov_b32_e32 v172, v125
	v_mov_b32_dpp v133, v129 quad_perm:[2,3,0,1] row_mask:0xf bank_mask:0xf
	v_pk_add_f32 v[128:129], v[132:133], v[128:129]
	v_mov_b32_e32 v190, v162
	v_pk_add_f32 v[124:125], v[172:173], v[128:129]
	v_pk_mul_f32 v[132:133], v[172:173], v[128:129]
	v_pk_fma_f32 v[128:129], v[172:173], v[128:129], v[174:175] neg_lo:[1,0,0] neg_hi:[1,0,0]
	v_sub_f32_e32 v115, v198, v133
	v_mul_f32_e32 v117, v129, v129
	v_fmac_f32_e32 v117, v115, v115
	v_sub_f32_e32 v119, v177, v133
	v_fmac_f32_e32 v117, v119, v119
	v_sub_f32_e32 v121, v163, v133
	v_fmac_f32_e32 v117, v121, v121
	v_sub_f32_e32 v123, v159, v133
	v_fmac_f32_e32 v117, v123, v123
	v_sub_f32_e32 v127, v179, v133
	v_fmac_f32_e32 v117, v127, v127
	v_sub_f32_e32 v135, v181, v133
	v_fmac_f32_e32 v117, v135, v135
	v_sub_f32_e32 v137, v183, v133
	v_fmac_f32_e32 v117, v137, v137
	v_sub_f32_e32 v152, v153, v133
	v_fmac_f32_e32 v117, v152, v152
	v_sub_f32_e32 v153, v157, v133
	v_mov_b32_e32 v125, v133
	v_mov_b32_dpp v190, v124 quad_perm:[1,0,3,2] row_mask:0xf bank_mask:0xf
	v_fmac_f32_e32 v117, v153, v153
	v_sub_f32_e32 v156, v161, v133
	v_pk_add_f32 v[130:131], v[130:131], v[132:133] op_sel:[0,1] neg_lo:[0,1] neg_hi:[0,1]
	v_fmac_f32_e32 v117, v156, v156
	v_pk_mul_f32 v[140:141], v[130:131], v[130:131]
	v_sub_f32_e32 v139, v139, v133
	v_sub_f32_e32 v157, v193, v133
	v_pk_add_f32 v[132:133], v[190:191], v[124:125] neg_lo:[0,1] neg_hi:[0,1]
	v_add_f32_e32 v117, v140, v117
	v_mov_b32_e32 v138, v133
	v_add_f32_e32 v117, v141, v117
	v_pk_mul_f32 v[140:141], v[138:139], v[138:139]
	v_pk_add_f32 v[124:125], v[124:125], v[190:191]
	v_add_f32_e32 v117, v141, v117
	v_add_f32_e32 v117, v140, v117
	v_fmac_f32_e32 v117, v157, v157
	v_mov_b64_e32 v[160:161], v[108:109]
	v_lshl_add_u64 v[164:165], v[164:165], 0, s[10:11]
	v_add_f32_dpp v117, v117, v117 quad_perm:[1,0,3,2] row_mask:0xf bank_mask:0xf bound_ctrl:1
	v_lshl_add_u64 v[170:171], v[170:171], 0, s[12:13]
	v_mov_b64_e32 v[158:159], v[106:107]
	v_add_f32_dpp v117, v117, v117 quad_perm:[2,3,0,1] row_mask:0xf bank_mask:0xf bound_ctrl:1
	v_fmamk_f32 v117, v117, 0x3c800000, v1
	v_mul_f32_e32 v128, 0x4f800000, v117
	v_cmp_gt_f32_e32 vcc, s8, v117
	s_nop 1
	v_cndmask_b32_e32 v117, v117, v128, vcc
	v_sqrt_f32_e32 v128, v117
	s_nop 0
	v_add_u32_e32 v138, -1, v128
	v_fma_f32 v140, -v138, v128, v117
	v_cmp_ge_f32_e64 s[0:1], 0, v140
	v_add_u32_e32 v140, 1, v128
	s_nop 0
	v_cndmask_b32_e64 v138, v128, v138, s[0:1]
	v_fma_f32 v128, -v140, v128, v117
	v_cmp_lt_f32_e64 s[0:1], 0, v128
	s_nop 1
	v_cndmask_b32_e64 v128, v138, v140, s[0:1]
	v_mul_f32_e32 v138, 0x37800000, v128
	v_cndmask_b32_e32 v128, v128, v138, vcc
	v_cmp_class_f32_e32 vcc, v117, v52
	v_mov_b32_e32 v140, v162
	s_nop 0
	v_cndmask_b32_e32 v117, v128, v117, vcc
	v_div_scale_f32 v128, s[0:1], v117, v117, 1.0
	v_rcp_f32_e32 v138, v128
	v_mov_b32_dpp v140, v124 quad_perm:[2,3,0,1] row_mask:0xf bank_mask:0xf
	v_fma_f32 v141, -v128, v138, 1.0
	v_fmac_f32_e32 v138, v141, v138
	v_div_scale_f32 v141, vcc, 1.0, v117, 1.0
	v_mul_f32_e32 v143, v141, v138
	v_fma_f32 v145, -v128, v143, v141
	v_fmac_f32_e32 v143, v145, v138
	v_fma_f32 v128, -v128, v143, v141
	v_div_fmas_f32 v128, v128, v138, v143
	v_div_fixup_f32 v141, v128, v117, 1.0
	v_pk_add_f32 v[124:125], v[124:125], v[140:141]
	v_mov_b32_e32 v124, v242
	v_pk_mul_f32 v[132:133], v[132:133], v[140:141]
	v_mul_f32_e32 v175, v115, v141
	v_mov_b32_e32 v125, v133
	v_mov_b32_e32 v132, v124
	v_mov_b32_e32 v133, v26
	v_pk_mul_f32 v[132:133], v[132:133], v[174:175]
	v_mul_f32_e32 v151, v129, v141
	v_add_f32_e32 v115, v30, v133
	v_mov_b32_e32 v128, v124
	v_mov_b32_e32 v129, v27
	v_add_f32_e32 v115, v132, v115
	v_pk_mul_f32 v[128:129], v[128:129], v[150:151]
	v_mul_f32_e32 v132, v115, v199
	v_add_f32_e32 v115, v31, v129
	v_add_f32_e32 v115, v128, v115
	v_mul_f32_e32 v155, v119, v141
	v_mov_b32_e32 v128, v124
	v_mov_b32_e32 v129, v28
	v_pk_mul_f32 v[128:129], v[128:129], v[154:155]
	v_mul_f32_e32 v133, v115, v200
	v_add_f32_e32 v115, v32, v129
	v_add_f32_e32 v115, v128, v115
	v_mul_f32_e32 v147, v121, v141
	v_mov_b32_e32 v128, v124
	v_mov_b32_e32 v129, v29
	v_pk_mul_f32 v[128:129], v[128:129], v[146:147]
	v_mul_f32_e32 v138, v115, v202
	v_add_f32_e32 v115, v33, v129
	v_add_f32_e32 v115, v128, v115
	v_mul_f32_e32 v149, v123, v141
	v_mov_b32_e32 v128, v124
	v_mov_b32_e32 v129, v34
	v_pk_mul_f32 v[128:129], v[128:129], v[148:149]
	v_mul_f32_e32 v140, v115, v203
	v_add_f32_e32 v115, v38, v129
; #define GAS __attribute__((address_space(1)))
; __device__ __forceinline__ void p5_post(Frame& F0, const In& I) {
;     ...
;     if (gw < T) P5_LOAD(gw);
;     ...
;         for (int e = 0; e < 16; ++e) o[e] = (y[e] * rstd * p_lw[e] + p_lb[e] + bs * vv[e]) * gg[e];
;         { unsigned w8[4];
; #pragma unroll
;           for (int q = 0; q < 4; ++q) { int t8 = __builtin_amdgcn_cvt_pk_fp8_f32(o[4 * q] * ACT8_SCALE, o[4 * q + 1] * ACT8_SCALE, 0, false); t8 = __builtin_amdgcn_cvt_pk_fp8_f32(o[4 * q + 2] * ACT8_SCALE, o[4 * q + 3] * ACT8_SCALE, t8, true); w8[q] = (unsigned)t8; }
;           *(GAS v4u*)((unsigned char*)YB + (size_t)tok * RW + c0) = (v4u){w8[0], w8[1], w8[2], w8[3]}; }
	v_add_f32_e32 v115, v128, v115
	v_mul_f32_e32 v143, v127, v141
	v_mov_b32_e32 v128, v124
	v_mov_b32_e32 v129, v35
	v_pk_mul_f32 v[128:129], v[128:129], v[142:143]
	v_mul_f32_e32 v146, v115, v208
	v_add_f32_e32 v115, v39, v129
	v_add_f32_e32 v115, v128, v115
	v_mul_f32_e32 v145, v135, v141
	v_mov_b32_e32 v128, v124
	v_mov_b32_e32 v129, v36
	v_pk_mul_f32 v[128:129], v[128:129], v[144:145]
	v_mul_f32_e32 v142, v115, v209
	v_add_f32_e32 v115, v40, v129
	v_add_f32_e32 v115, v128, v115
	v_mul_f32_e32 v135, v137, v141
	v_mov_b32_e32 v128, v124
	v_mov_b32_e32 v129, v37
	v_pk_mul_f32 v[128:129], v[128:129], v[134:135]
	v_mul_f32_e32 v143, v115, v211
	v_add_f32_e32 v115, v41, v129
	v_add_f32_e32 v115, v128, v115
	v_mul_f32_e32 v137, v152, v141
	v_mov_b32_e32 v128, v124
	v_mov_b32_e32 v129, v42
	v_pk_mul_f32 v[128:129], v[128:129], v[136:137]
	v_mul_f32_e32 v134, v115, v212
	v_add_f32_e32 v115, v46, v129
	v_add_f32_e32 v115, v128, v115
	v_mul_f32_e32 v127, v153, v141
	v_mov_b32_e32 v128, v124
	v_mov_b32_e32 v129, v43
	v_pk_mul_f32 v[126:127], v[128:129], v[126:127]
	v_mul_f32_e32 v135, v115, v219
	v_add_f32_e32 v115, v47, v127
	v_add_f32_e32 v115, v126, v115
	v_mul_f32_e32 v123, v156, v141
	v_mov_b32_e32 v126, v124
	v_mov_b32_e32 v127, v44
	v_pk_mul_f32 v[122:123], v[126:127], v[122:123]
	v_mul_f32_e32 v128, v115, v220
	v_add_f32_e32 v115, v48, v123
	v_add_f32_e32 v115, v122, v115
	v_mul_f32_e32 v126, v115, v223
	v_mul_f32_e32 v115, v130, v141
	v_mov_b32_e32 v122, v124
	v_mov_b32_e32 v123, v45
	v_pk_mul_f32 v[114:115], v[122:123], v[114:115]
	v_mul_f32_e32 v121, v131, v141
	v_add_f32_e32 v115, v49, v115
	v_add_f32_e32 v114, v114, v115
	v_mul_f32_e32 v122, v114, v224
	v_mov_b32_e32 v114, v124
	v_mov_b32_e32 v115, v50
	v_pk_mul_f32 v[114:115], v[114:115], v[120:121]
	v_mul_f32_e32 v117, v139, v141
	v_add_f32_e32 v115, v54, v115
	v_add_f32_e32 v114, v114, v115
	v_mul_f32_e32 v120, v114, v225
	v_mov_b32_e32 v114, v124
	v_mov_b32_e32 v115, v51
	v_pk_mul_f32 v[114:115], v[114:115], v[116:117]
	v_mul_f32_e32 v119, v157, v141
	v_add_f32_e32 v115, v55, v115
	v_add_f32_e32 v114, v114, v115
	v_mul_f32_e32 v117, v114, v226
	v_pk_mul_f32 v[114:115], v[124:125], v[168:169]
	v_mov_b32_e32 v125, v53
	v_add_f32_e32 v115, v56, v115
	v_add_f32_e32 v114, v114, v115
	v_mul_f32_e32 v121, v114, v227
	v_pk_mul_f32 v[114:115], v[124:125], v[118:119]
	v_mul_f32_e32 v116, 0x41800000, v133
	v_add_f32_e32 v115, v57, v115
	v_add_f32_e32 v114, v114, v115
	v_mul_f32_e32 v118, v114, v228
	v_mul_f32_e32 v115, 0x41800000, v132
	v_mov_b32_e32 v114, v162
	v_cvt_pk_fp8_f32 v114, v115, v116
	v_mul_f32_e32 v123, 0x41800000, v146
	v_mul_f32_e32 v124, 0x41800000, v142
	v_mov_b32_e32 v115, v162
	v_cvt_pk_fp8_f32 v115, v123, v124
	v_mul_f32_e32 v116, 0x41800000, v138
	v_mul_f32_e32 v119, 0x41800000, v140
	v_cvt_pk_fp8_f32 v114, v116, v119 op_sel:[0,0,1]
	v_mul_f32_e32 v116, 0x41800000, v143
	v_mul_f32_e32 v119, 0x41800000, v134
	v_cvt_pk_fp8_f32 v115, v116, v119 op_sel:[0,0,1]
	v_mul_f32_e32 v119, 0x41800000, v135
	v_mul_f32_e32 v123, 0x41800000, v128
	v_mov_b32_e32 v116, v162
	v_cvt_pk_fp8_f32 v116, v119, v123
	v_mul_f32_e32 v120, 0x41800000, v120
	v_mul_f32_e32 v123, 0x41800000, v117
	v_mov_b32_e32 v117, v162
	v_cvt_pk_fp8_f32 v117, v120, v123
	v_mul_f32_e32 v119, 0x41800000, v126
	v_mul_f32_e32 v122, 0x41800000, v122
	v_cvt_pk_fp8_f32 v116, v119, v122 op_sel:[0,0,1]
	v_mul_f32_e32 v119, 0x41800000, v121
	v_mul_f32_e32 v118, 0x41800000, v118
	v_cvt_pk_fp8_f32 v117, v119, v118 op_sel:[0,0,1]
	v_lshl_add_u64 v[118:119], s[96:97], 0, v[166:167]
	v_mov_b32_e32 v242, v240
	v_mov_b64_e32 v[136:137], v[68:69]
	v_mov_b64_e32 v[144:145], v[76:77]
	global_store_dwordx4 v[118:119], v[114:117], off
	v_mov_b64_e32 v[120:121], v[80:81]
	v_mov_b64_e32 v[148:149], v[84:85]
	v_mov_b64_e32 v[116:117], v[72:73]
	v_mov_b64_e32 v[124:125], v[88:89]
	v_mov_b64_e32 v[152:153], v[92:93]
	v_mov_b64_e32 v[128:129], v[96:97]
	v_mov_b64_e32 v[156:157], v[100:101]
	v_mov_b64_e32 v[132:133], v[104:105]
	v_mov_b64_e32 v[140:141], v[112:113]
	v_lshl_add_u64 v[166:167], v[166:167], 0, s[6:7]
	s_andn2_b64 vcc, exec, s[24:25]
	v_mov_b64_e32 v[134:135], v[66:67]
	v_mov_b64_e32 v[114:115], v[70:71]
	v_mov_b64_e32 v[142:143], v[74:75]
	v_mov_b64_e32 v[118:119], v[78:79]
	v_mov_b64_e32 v[146:147], v[82:83]
	v_mov_b64_e32 v[122:123], v[86:87]
	v_mov_b64_e32 v[150:151], v[90:91]
	v_mov_b64_e32 v[126:127], v[94:95]
	v_mov_b64_e32 v[154:155], v[98:99]
	v_mov_b64_e32 v[130:131], v[102:103]
	v_mov_b64_e32 v[138:139], v[110:111]
	s_cbranch_vccz .LBB0_1216
.LBB0_1214:
	s_add_i32 s2, s2, s68
	s_cmpk_gt_i32 s2, 0x7fff
	s_cselect_b64 s[24:25], -1, 0
	s_and_b64 vcc, exec, s[24:25]
	s_cbranch_vccnz .LBB0_1213
	v_lshl_add_u64 v[98:99], s[96:97], 0, v[170:171]
	v_add_co_u32_e32 v66, vcc, 0x90000000, v98
	v_lshl_add_u64 v[100:101], s[96:97], 0, v[164:165]
	s_nop 0
	v_addc_co_u32_e32 v67, vcc, 0, v99, vcc
	v_add_co_u32_e32 v72, vcc, 0x84000000, v98
	v_lshl_add_u64 v[86:87], v[100:101], 0, s[16:17]
	s_nop 0
	v_addc_co_u32_e32 v73, vcc, 0, v99, vcc
	v_add_co_u32_e32 v88, vcc, 0x6e000000, v100
	v_lshl_add_u64 v[94:95], v[100:101], 0, s[18:19]
	s_nop 0
	v_addc_co_u32_e32 v89, vcc, 0, v101, vcc
	v_lshl_add_u64 v[102:103], v[100:101], 0, s[20:21]
	v_add_co_u32_e32 v100, vcc, s3, v100
	v_lshl_add_u64 v[70:71], v[98:99], 0, s[4:5]
	s_nop 0
	v_addc_co_u32_e32 v101, vcc, 0, v101, vcc
	v_add_co_u32_e32 v104, vcc, 0x8c000000, v98
	v_lshl_add_u64 v[78:79], v[98:99], 0, s[14:15]
	v_lshl_add_u64 v[110:111], v[98:99], 0, s[22:23]
	v_addc_co_u32_e32 v105, vcc, 0, v99, vcc
	s_lshl_b32 s98, s2, 6
	s_add_u32 s98, s100, s98
	s_addc_u32 s99, s101, 0
	global_load_dword v240, v241, s[98:99]
	global_load_dwordx4 v[66:69], v[66:67], off
	s_nop 0
	s_nop 0
	global_load_dwordx4 v[70:73], v[70:71], off offset:16
	s_nop 0
	s_nop 0
	s_nop 0
	s_nop 0
	s_nop 0
	global_load_dwordx4 v[98:101], v[100:101], off
	s_nop 0
	global_load_dwordx4 v[106:109], v[104:105], off
	s_nop 0
	global_load_dwordx4 v[102:105], v[102:103], off offset:16
	s_nop 0
	global_load_dwordx4 v[110:113], v[110:111], off offset:16
	s_branch .LBB0_1213
